# cq loaded in phase 0 (ahead of the halo DMA) so the phase-1 epilogue no longer waits for the halo; halo wait moved to just before barrier 1
# speedup vs baseline: 1.0229x; 1.0229x over previous
_Z7na_mainPKDF16_PKhS0_PKfS4_S4_S4_Pf:
	s_lshl_b32 s3, s2, 5
	s_and_b32 s3, s3, 0xe0
	s_ashr_i32 s2, s2, 3
	s_add_i32 s3, s3, s2
	s_ashr_i32 s2, s3, 6
	s_lshl_b32 s3, s3, 5
	s_and_b32 s14, s3, 0x7e0
	v_mov_b32_e32 v1, 0x7c0
	s_load_dwordx8 s[4:11], s[0:1], 0x0
	s_load_dwordx2 s[18:19], s[0:1], 0x20
	v_med3_u32 v1, s14, 32, v1
	v_subrev_u32_e32 v97, 32, v1
	s_ashr_i32 s3, s2, 31
	v_lshlrev_b32_e32 v58, 1, v97
	s_lshl_b64 s[12:13], s[2:3], 12
	v_mov_b32_e32 v59, 0
	v_sub_u32_e32 v60, s14, v97
	v_lshl_add_u64 v[10:11], s[12:13], 0, v[58:59]
	v_lshlrev_b64 v[2:3], 9, v[10:11]
	v_lshl_or_b32 v22, v60, 6, v0
	s_waitcnt lgkmcnt(0)
	v_and_b32_e32 v208, 31, v0
	v_lshlrev_b32_e32 v208, 5, v208
	global_load_dwordx4 v[192:195], v208, s[18:19]
	global_load_dwordx4 v[196:199], v208, s[18:19] offset:16
	v_lshl_add_u64 v[20:21], s[4:5], 0, v[2:3]
	v_ashrrev_i32_e32 v23, 31, v22
	v_lshl_add_u64 v[2:3], v[22:23], 4, v[20:21]
	global_load_dwordx4 v[12:15], v[2:3], off
	v_or_b32_e32 v28, 0x200, v22
	v_ashrrev_i32_e32 v29, 31, v28
	v_lshl_add_u64 v[2:3], v[28:29], 4, v[20:21]
	global_load_dwordx4 v[16:19], v[2:3], off
	v_or_b32_e32 v184, 0x400, v22
	v_ashrrev_i32_e32 v185, 31, v184
	v_lshl_add_u64 v[184:185], v[184:185], 4, v[20:21]
	v_or_b32_e32 v188, 0x600, v22
	v_ashrrev_i32_e32 v189, 31, v188
	v_lshl_add_u64 v[188:189], v[188:189], 4, v[20:21]
	global_load_dwordx4 v[184:187], v[184:185], off
	global_load_dwordx4 v[188:191], v[188:189], off
	v_lshrrev_b32_e32 v99, 6, v0
	v_and_b32_e32 v98, 63, v0
	v_lshlrev_b32_e32 v118, 13, v99
	v_lshl_or_b32 v58, v98, 5, v118
	s_movk_i32 s15, 0x1000
	v_lshl_add_u64 v[24:25], s[6:7], 0, v[58:59]
	v_or_b32_e32 v32, 0x400, v22
	v_or_b32_e32 v62, 0x600, v22
	v_add_co_u32_e32 v64, vcc, s15, v24
	s_mov_b64 s[12:13], 0x1000
	s_mov_b64 s[16:17], 0x1800
	v_lshlrev_b32_e32 v72, 1, v60
	v_lshrrev_b32_e32 v23, 5, v22
	v_and_b32_e32 v34, 32, v22
	v_ashrrev_i32_e32 v33, 31, v32
	v_ashrrev_i32_e32 v63, 31, v62
	v_addc_co_u32_e32 v65, vcc, 0, v25, vcc
	global_load_dwordx4 v[6:9], v58, s[6:7] offset:16
	global_load_dwordx4 v[2:5], v58, s[6:7]
	global_load_dwordx4 v[54:57], v58, s[6:7] offset:2064
	global_load_dwordx4 v[50:53], v58, s[6:7] offset:2048
	v_lshrrev_b32_e32 v58, 6, v22
	v_bfe_u32 v73, v22, 8, 2
	v_lshl_add_u64 v[26:27], v[24:25], 0, s[12:13]
	v_lshl_add_u64 v[24:25], v[24:25], 0, s[16:17]
	v_cmp_ne_u32_e32 vcc, 0, v34
	v_sub_u32_e32 v75, v23, v72
	global_load_dwordx4 v[42:45], v[64:65], off
	global_load_dwordx4 v[46:49], v[26:27], off offset:16
	global_load_dwordx4 v[34:37], v[64:65], off offset:2048
	global_load_dwordx4 v[38:41], v[24:25], off offset:16
	v_mov_b32_e32 v61, 0x60
	v_cndmask_b32_e32 v74, 0, v61, vcc
	v_add_u32_e32 v33, v74, v58
	v_lshlrev_b32_e32 v64, 2, v33
	v_bfe_u32 v96, v0, 4, 1
	v_and_b32_e32 v100, 15, v0
	v_mov_b32_e32 v30, v59
	v_mov_b32_e32 v31, v59
	v_and_b32_e32 v64, 12, v64
	v_mul_u32_u24_e32 v29, 0xc000, v96
	v_bitop3_b32 v64, v64, v100, v73 bitop3:0x36
	v_lshl_or_b32 v64, v64, 4, v29
	v_lshlrev_b32_e32 v63, 1, v75
	v_lshl_add_u32 v33, v33, 8, v64
	v_bfe_u32 v71, v0, 1, 4
	v_and_b32_e32 v70, 32, v0
	v_lshlrev_b32_e32 v1, 3, v0
	v_lshrrev_b32_e32 v58, 1, v75
	v_and_b32_e32 v1, 8, v1
	v_add_lshl_u32 v58, v58, v70, 8
	v_lshlrev_b32_e32 v121, 3, v99
	v_bfe_u32 v101, v0, 4, 2
	v_lshlrev_b32_e32 v102, 2, v101
	v_and_b32_e32 v116, 31, v0
	v_bfe_u32 v119, v0, 5, 1
	v_lshlrev_b32_e32 v124, 1, v119
	v_lshlrev_b32_e32 v117, 8, v116
	v_lshrrev_b32_e32 v95, 4, v0
	s_movk_i32 s16, 0x60
	s_mov_b32 s17, 0xc000
	v_and_b32_e32 v211, 3, v99
	v_lshrrev_b32_e32 v212, 2, v99
	v_lshl_or_b32 v211, v211, 2, v212
	v_xor_b32_e32 v213, v100, v211
	v_mul_u32_u24_e32 v214, 0x60, v119
	v_add3_u32 v214, v214, v60, v99
	v_mul_u32_u24_e32 v215, 0xc000, v96
	v_lshl_add_u32 v214, v214, 8, v215
	v_lshl_or_b32 v220, v213, 4, v214
	v_xor_b32_e32 v221, 32, v220
	v_xor_b32_e32 v216, v71, v211
	v_lshl_add_u32 v217, v119, 5, v99
	v_lshlrev_b32_e32 v217, 8, v217
	v_lshl_or_b32 v216, v216, 4, v217
	v_or_b32_e32 v216, v216, v1
	v_add_u32_e32 v222, 0x23800, v216
	v_xor_b32_e32 v223, 32, v222
	s_waitcnt vmcnt(11)
	ds_write_b128 v220, v[12:15]
	v_fma_mix_f32 v200, v192, v12, 0 op_sel_hi:[0,1,0]
	v_fma_mix_f32 v201, v193, v12, 0 op_sel:[0,1,0] op_sel_hi:[0,1,0]
	v_cvt_f32_f16_e32 v211, v12
	v_cvt_f32_f16_sdwa v212, v12 dst_sel:DWORD dst_unused:UNUSED_PAD src0_sel:WORD_1
	v_fma_mix_f32 v200, v194, v13, v200 op_sel_hi:[0,1,0]
	v_fma_mix_f32 v201, v195, v13, v201 op_sel:[0,1,0] op_sel_hi:[0,1,0]
	v_cvt_f32_f16_e32 v213, v13
	v_cvt_f32_f16_sdwa v214, v13 dst_sel:DWORD dst_unused:UNUSED_PAD src0_sel:WORD_1
	v_fma_mix_f32 v200, v196, v14, v200 op_sel_hi:[0,1,0]
	v_fma_mix_f32 v201, v197, v14, v201 op_sel:[0,1,0] op_sel_hi:[0,1,0]
	v_cvt_f32_f16_e32 v215, v14
	v_cvt_f32_f16_sdwa v216, v14 dst_sel:DWORD dst_unused:UNUSED_PAD src0_sel:WORD_1
	v_fma_mix_f32 v200, v198, v15, v200 op_sel_hi:[0,1,0]
	v_fma_mix_f32 v201, v199, v15, v201 op_sel:[0,1,0] op_sel_hi:[0,1,0]
	v_cvt_f32_f16_e32 v217, v15
	v_cvt_f32_f16_sdwa v218, v15 dst_sel:DWORD dst_unused:UNUSED_PAD src0_sel:WORD_1
	v_cvt_pk_fp8_f32 v224, v211, v212
	v_cvt_pk_fp8_f32 v225, v215, v216
	v_cvt_pk_fp8_f32 v224, v213, v214 op_sel:[0,0,1]
	v_cvt_pk_fp8_f32 v225, v217, v218 op_sel:[0,0,1]
	s_nop 0
	ds_write_b64 v222, v[224:225]
	s_waitcnt vmcnt(10)
	ds_write_b128 v221, v[16:19] offset:2048
	v_fma_mix_f32 v202, v192, v16, 0 op_sel_hi:[0,1,0]
	v_fma_mix_f32 v203, v193, v16, 0 op_sel:[0,1,0] op_sel_hi:[0,1,0]
	v_cvt_f32_f16_e32 v211, v16
	v_cvt_f32_f16_sdwa v212, v16 dst_sel:DWORD dst_unused:UNUSED_PAD src0_sel:WORD_1
	v_fma_mix_f32 v202, v194, v17, v202 op_sel_hi:[0,1,0]
	v_fma_mix_f32 v203, v195, v17, v203 op_sel:[0,1,0] op_sel_hi:[0,1,0]
	v_cvt_f32_f16_e32 v213, v17
	v_cvt_f32_f16_sdwa v214, v17 dst_sel:DWORD dst_unused:UNUSED_PAD src0_sel:WORD_1
	v_fma_mix_f32 v202, v196, v18, v202 op_sel_hi:[0,1,0]
	v_fma_mix_f32 v203, v197, v18, v203 op_sel:[0,1,0] op_sel_hi:[0,1,0]
	v_cvt_f32_f16_e32 v215, v18
	v_cvt_f32_f16_sdwa v216, v18 dst_sel:DWORD dst_unused:UNUSED_PAD src0_sel:WORD_1
	v_fma_mix_f32 v202, v198, v19, v202 op_sel_hi:[0,1,0]
	v_fma_mix_f32 v203, v199, v19, v203 op_sel:[0,1,0] op_sel_hi:[0,1,0]
	v_cvt_f32_f16_e32 v217, v19
	v_cvt_f32_f16_sdwa v218, v19 dst_sel:DWORD dst_unused:UNUSED_PAD src0_sel:WORD_1
	v_cvt_pk_fp8_f32 v226, v211, v212
	v_cvt_pk_fp8_f32 v227, v215, v216
	v_cvt_pk_fp8_f32 v226, v213, v214 op_sel:[0,0,1]
	v_cvt_pk_fp8_f32 v227, v217, v218 op_sel:[0,0,1]
	s_nop 0
	ds_write_b64 v223, v[226:227] offset:2048
	s_waitcnt vmcnt(9)
	ds_write_b128 v220, v[184:187] offset:4096
	v_fma_mix_f32 v204, v192, v184, 0 op_sel_hi:[0,1,0]
	v_fma_mix_f32 v205, v193, v184, 0 op_sel:[0,1,0] op_sel_hi:[0,1,0]
	v_cvt_f32_f16_e32 v211, v184
	v_cvt_f32_f16_sdwa v212, v184 dst_sel:DWORD dst_unused:UNUSED_PAD src0_sel:WORD_1
	v_fma_mix_f32 v204, v194, v185, v204 op_sel_hi:[0,1,0]
	v_fma_mix_f32 v205, v195, v185, v205 op_sel:[0,1,0] op_sel_hi:[0,1,0]
	v_cvt_f32_f16_e32 v213, v185
	v_cvt_f32_f16_sdwa v214, v185 dst_sel:DWORD dst_unused:UNUSED_PAD src0_sel:WORD_1
	v_fma_mix_f32 v204, v196, v186, v204 op_sel_hi:[0,1,0]
	v_fma_mix_f32 v205, v197, v186, v205 op_sel:[0,1,0] op_sel_hi:[0,1,0]
	v_cvt_f32_f16_e32 v215, v186
	v_cvt_f32_f16_sdwa v216, v186 dst_sel:DWORD dst_unused:UNUSED_PAD src0_sel:WORD_1
	v_fma_mix_f32 v204, v198, v187, v204 op_sel_hi:[0,1,0]
	v_fma_mix_f32 v205, v199, v187, v205 op_sel:[0,1,0] op_sel_hi:[0,1,0]
	v_cvt_f32_f16_e32 v217, v187
	v_cvt_f32_f16_sdwa v218, v187 dst_sel:DWORD dst_unused:UNUSED_PAD src0_sel:WORD_1
	v_cvt_pk_fp8_f32 v228, v211, v212
	v_cvt_pk_fp8_f32 v229, v215, v216
	v_cvt_pk_fp8_f32 v228, v213, v214 op_sel:[0,0,1]
	v_cvt_pk_fp8_f32 v229, v217, v218 op_sel:[0,0,1]
	s_nop 0
	ds_write_b64 v222, v[228:229] offset:4096
	s_waitcnt vmcnt(8)
	ds_write_b128 v221, v[188:191] offset:6144
	v_fma_mix_f32 v206, v192, v188, 0 op_sel_hi:[0,1,0]
	v_fma_mix_f32 v207, v193, v188, 0 op_sel:[0,1,0] op_sel_hi:[0,1,0]
	v_cvt_f32_f16_e32 v211, v188
	v_cvt_f32_f16_sdwa v212, v188 dst_sel:DWORD dst_unused:UNUSED_PAD src0_sel:WORD_1
	v_fma_mix_f32 v206, v194, v189, v206 op_sel_hi:[0,1,0]
	v_fma_mix_f32 v207, v195, v189, v207 op_sel:[0,1,0] op_sel_hi:[0,1,0]
	v_cvt_f32_f16_e32 v213, v189
	v_cvt_f32_f16_sdwa v214, v189 dst_sel:DWORD dst_unused:UNUSED_PAD src0_sel:WORD_1
	v_fma_mix_f32 v206, v196, v190, v206 op_sel_hi:[0,1,0]
	v_fma_mix_f32 v207, v197, v190, v207 op_sel:[0,1,0] op_sel_hi:[0,1,0]
	v_cvt_f32_f16_e32 v215, v190
	v_cvt_f32_f16_sdwa v216, v190 dst_sel:DWORD dst_unused:UNUSED_PAD src0_sel:WORD_1
	v_fma_mix_f32 v206, v198, v191, v206 op_sel_hi:[0,1,0]
	v_fma_mix_f32 v207, v199, v191, v207 op_sel:[0,1,0] op_sel_hi:[0,1,0]
	v_cvt_f32_f16_e32 v217, v191
	v_cvt_f32_f16_sdwa v218, v191 dst_sel:DWORD dst_unused:UNUSED_PAD src0_sel:WORD_1
	v_cvt_pk_fp8_f32 v230, v211, v212
	v_cvt_pk_fp8_f32 v231, v215, v216
	v_cvt_pk_fp8_f32 v230, v213, v214 op_sel:[0,0,1]
	v_cvt_pk_fp8_f32 v231, v217, v218 op_sel:[0,0,1]
	s_nop 0
	ds_write_b64 v223, v[230:231] offset:6144
	v_add_f32_e32 v200, v200, v201
	v_add_f32_e32 v202, v202, v203
	v_add_f32_e32 v204, v204, v205
	v_add_f32_e32 v206, v206, v207
	v_lshlrev_b32_e32 v208, 7, v119
	v_lshl_add_u32 v208, v99, 2, v208
	v_add_u32_e32 v208, 0x27800, v208
	v_add_f32_dpp v200, v200, v200 quad_perm:[1,0,3,2] row_mask:0xf bank_mask:0xf
	v_add_f32_dpp v202, v202, v202 quad_perm:[1,0,3,2] row_mask:0xf bank_mask:0xf
	v_add_f32_dpp v204, v204, v204 quad_perm:[1,0,3,2] row_mask:0xf bank_mask:0xf
	v_add_f32_dpp v206, v206, v206 quad_perm:[1,0,3,2] row_mask:0xf bank_mask:0xf
	v_add_f32_dpp v200, v200, v200 quad_perm:[2,3,0,1] row_mask:0xf bank_mask:0xf
	v_add_f32_dpp v202, v202, v202 quad_perm:[2,3,0,1] row_mask:0xf bank_mask:0xf
	v_add_f32_dpp v204, v204, v204 quad_perm:[2,3,0,1] row_mask:0xf bank_mask:0xf
	v_add_f32_dpp v206, v206, v206 quad_perm:[2,3,0,1] row_mask:0xf bank_mask:0xf
	v_add_f32_dpp v200, v200, v200 row_half_mirror row_mask:0xf bank_mask:0xf
	v_add_f32_dpp v202, v202, v202 row_half_mirror row_mask:0xf bank_mask:0xf
	v_add_f32_dpp v204, v204, v204 row_half_mirror row_mask:0xf bank_mask:0xf
	v_add_f32_dpp v206, v206, v206 row_half_mirror row_mask:0xf bank_mask:0xf
	v_add_f32_dpp v200, v200, v200 row_mirror row_mask:0xf bank_mask:0xf
	v_add_f32_dpp v202, v202, v202 row_mirror row_mask:0xf bank_mask:0xf
	v_add_f32_dpp v204, v204, v204 row_mirror row_mask:0xf bank_mask:0xf
	v_add_f32_dpp v206, v206, v206 row_mirror row_mask:0xf bank_mask:0xf
	v_add_f32_dpp v200, v200, v200 row_bcast:15 row_mask:0xa bank_mask:0xf
	v_add_f32_dpp v202, v202, v202 row_bcast:15 row_mask:0xa bank_mask:0xf
	v_add_f32_dpp v204, v204, v204 row_bcast:15 row_mask:0xa bank_mask:0xf
	v_add_f32_dpp v206, v206, v206 row_bcast:15 row_mask:0xa bank_mask:0xf
	s_mov_b32 exec_lo, 0xffff0000
	s_mov_b32 exec_hi, 0xffff0000
	ds_write_b32 v208, v200
	ds_write_b32 v208, v202 offset:32
	ds_write_b32 v208, v204 offset:64
	ds_write_b32 v208, v206 offset:96
	s_mov_b64 exec, -1
	v_lshlrev_b32_e32 v201, 7, v99
	v_lshl_or_b32 v201, v119, 4, v201
	global_load_dwordx4 v[184:187], v201, s[10:11]
	global_load_dwordx4 v[188:191], v201, s[10:11] offset:32
	global_load_dwordx4 v[192:195], v201, s[10:11] offset:64
	global_load_dwordx4 v[196:199], v201, s[10:11] offset:96
	v_cmp_lt_i32_e32 vcc, v121, v60
	s_nop 0
	v_mov_b32_e32 v15, v59
	v_cndmask_b32_e64 v12, 32, 0, vcc
	v_add_u32_e32 v16, v12, v121
	v_or_b32_e32 v12, v16, v101
	v_lshlrev_b32_e32 v58, 1, v12
	v_lshrrev_b32_e32 v12, 5, v0
	v_and_b32_e32 v12, 2, v12
	v_bitop3_b32 v14, v102, v100, v12 bitop3:0x36
	v_lshl_add_u64 v[12:13], v[10:11], 0, v[58:59]
	v_lshlrev_b64 v[12:13], 9, v[12:13]
	v_lshlrev_b32_e32 v16, 8, v16
	v_lshl_add_u64 v[12:13], s[4:5], 0, v[12:13]
	v_lshlrev_b32_e32 v14, 4, v14
	v_readfirstlane_b32 s6, v16
	v_add_u32_e32 v17, 0xc000, v16
	v_lshl_add_u64 v[12:13], v[12:13], 0, v[14:15]
	s_mov_b32 m0, s6
	s_mov_b64 s[6:7], 0x100
	v_readfirstlane_b32 s12, v17
	global_load_lds_dwordx4 v[12:13], off
	v_lshl_add_u64 v[12:13], v[12:13], 0, s[6:7]
	s_mov_b32 m0, s12
	v_or_b32_e32 v58, 1, v58
	global_load_lds_dwordx4 v[12:13], off
	v_lshl_add_u64 v[12:13], v[10:11], 0, v[58:59]
	v_lshlrev_b64 v[12:13], 9, v[12:13]
	v_lshl_add_u64 v[12:13], s[4:5], 0, v[12:13]
	v_lshl_add_u64 v[12:13], v[12:13], 0, v[14:15]
	v_add_u32_e32 v14, 0x6000, v16
	v_bfe_u32 v61, v0, 2, 2
	v_readfirstlane_b32 s12, v14
	v_add_u32_e32 v14, 0x12000, v16
	s_mov_b32 m0, s12
	v_readfirstlane_b32 s12, v14
	global_load_lds_dwordx4 v[12:13], off
	v_lshl_add_u64 v[12:13], v[12:13], 0, s[6:7]
	s_mov_b32 m0, s12
	v_add_u32_e32 v18, 0x23800, v117
	global_load_lds_dwordx4 v[12:13], off
	v_or_b32_e32 v12, 4, v121
	v_cmp_lt_i32_e32 vcc, v12, v60
	s_nop 1
	v_cndmask_b32_e64 v13, 32, 0, vcc
	v_add_u32_e32 v16, v13, v12
	v_or_b32_e32 v13, v16, v101
	v_lshlrev_b32_e32 v58, 1, v13
	v_bfe_u32 v12, v12, 2, 2
	v_bitop3_b32 v14, v102, v100, v12 bitop3:0x36
	v_lshl_add_u64 v[12:13], v[10:11], 0, v[58:59]
	v_lshlrev_b64 v[12:13], 9, v[12:13]
	v_lshlrev_b32_e32 v16, 8, v16
	v_lshl_add_u64 v[12:13], s[4:5], 0, v[12:13]
	v_lshlrev_b32_e32 v14, 4, v14
	v_readfirstlane_b32 s12, v16
	v_add_u32_e32 v17, 0xc000, v16
	v_lshl_add_u64 v[12:13], v[12:13], 0, v[14:15]
	s_mov_b32 m0, s12
	v_readfirstlane_b32 s12, v17
	v_or_b32_e32 v58, 1, v58
	global_load_lds_dwordx4 v[12:13], off
	v_lshl_add_u64 v[12:13], v[12:13], 0, s[6:7]
	s_mov_b32 m0, s12
	v_lshl_add_u64 v[10:11], v[10:11], 0, v[58:59]
	global_load_lds_dwordx4 v[12:13], off
	v_lshlrev_b64 v[10:11], 9, v[10:11]
	v_add_u32_e32 v12, 0x6000, v16
	v_lshl_add_u64 v[10:11], s[4:5], 0, v[10:11]
	v_readfirstlane_b32 s4, v12
	v_add_u32_e32 v12, 0x12000, v16
	v_lshl_add_u64 v[10:11], v[10:11], 0, v[14:15]
	s_mov_b32 m0, s4
	v_readfirstlane_b32 s4, v12
	global_load_lds_dwordx4 v[10:11], off
	v_lshl_add_u64 v[10:11], v[10:11], 0, s[6:7]
	s_mov_b32 m0, s4
	s_nop 0
	global_load_lds_dwordx4 v[10:11], off
	s_waitcnt lgkmcnt(0)
	s_barrier
	v_lshlrev_b32_e32 v10, 2, v0
	v_and_b32_e32 v94, 12, v10
	v_or_b32_e32 v120, v94, v61
	v_bitop3_b32 v10, v124, v94, v61 bitop3:0x1e
	v_lshl_or_b32 v14, v10, 4, v18
	v_bitop3_b32 v10, v124, v120, 1 bitop3:0x36
	v_lshl_or_b32 v19, v10, 4, v18
	s_load_dwordx4 s[4:7], s[0:1], 0x20
	s_load_dwordx2 s[12:13], s[0:1], 0x38
	ds_read_b128 v[10:13], v14
	ds_read_b128 v[62:65], v14 offset:8192
	ds_read_b128 v[14:17], v19
	ds_read_b128 v[66:69], v19 offset:8192
	v_bitop3_b32 v19, v124, v120, 4 bitop3:0x36
	v_lshl_or_b32 v19, v19, 4, v18
	v_bitop3_b32 v20, v124, v120, 5 bitop3:0x36
	v_lshl_or_b32 v20, v20, 4, v18
	ds_read_b128 v[70:73], v19
	ds_read_b128 v[78:81], v19 offset:8192
	ds_read_b128 v[74:77], v20
	ds_read_b128 v[82:85], v20 offset:8192
	v_bitop3_b32 v19, v124, v120, 8 bitop3:0x36
	v_lshl_or_b32 v19, v19, 4, v18
	v_bitop3_b32 v20, v124, v120, 9 bitop3:0x36
	v_lshl_or_b32 v20, v20, 4, v18
	ds_read_b128 v[86:89], v19
	ds_read_b128 v[104:107], v19 offset:8192
	ds_read_b128 v[90:93], v20
	ds_read_b128 v[108:111], v20 offset:8192
	v_bitop3_b32 v19, v124, v120, 12 bitop3:0x36
	v_lshl_or_b32 v19, v19, 4, v18
	v_bitop3_b32 v20, v124, v120, 13 bitop3:0x36
	v_lshl_or_b32 v18, v20, 4, v18
	ds_read_b128 v[126:129], v19
	ds_read_b128 v[134:137], v19 offset:8192
	ds_read_b128 v[130:133], v18
	ds_read_b128 v[138:141], v18 offset:8192
	v_mov_b32_e32 v103, 0x7f
	v_lshlrev_b32_e32 v58, 7, v99
	v_or_b32_e32 v122, 0x18000, v117
	s_waitcnt vmcnt(12) lgkmcnt(0)
	v_mfma_scale_f32_32x32x64_f8f6f4 v[18:33], v[2:9], v[10:17], 0, v103, v103 op_sel_hi:[0,0,0]
	v_lshlrev_b32_e32 v125, 3, v119
	v_or_b32_e32 v123, 0x1a000, v117
	v_mfma_scale_f32_32x32x64_f8f6f4 v[2:17], v[2:9], v[62:69], 0, v103, v103 op_sel_hi:[0,0,0]
	v_and_b32_e32 v62, 12, v95
	v_mfma_scale_f32_32x32x64_f8f6f4 v[18:33], v[50:57], v[70:77], v[18:33], v103, v103 op_sel_hi:[0,0,0]
	v_mfma_scale_f32_32x32x64_f8f6f4 v[2:17], v[50:57], v[78:85], v[2:17], v103, v103 op_sel_hi:[0,0,0]
	s_brev_b32 s10, 60
	v_lshlrev_b32_e32 v58, 6, v0
	v_and_b32_e32 v58, 0x4000, v58
	v_or3_b32 v63, v122, v58, v125
	v_or3_b32 v58, v123, v58, v125
	v_mfma_scale_f32_32x32x64_f8f6f4 v[18:33], v[42:49], v[86:93], v[18:33], v103, v103 op_sel_hi:[0,0,0]
	v_mfma_scale_f32_32x32x64_f8f6f4 v[2:17], v[42:49], v[104:111], v[2:17], v103, v103 op_sel_hi:[0,0,0]
	s_nop 0
	v_mfma_scale_f32_32x32x64_f8f6f4 v[2:17], v[34:41], v[134:141], v[2:17], v103, v103 op_sel_hi:[0,0,0]
	v_mfma_scale_f32_32x32x64_f8f6f4 v[18:33], v[34:41], v[126:133], v[18:33], v103, v103 op_sel_hi:[0,0,0]
	s_waitcnt vmcnt(8)
	s_nop 15
	s_nop 1
	v_fma_f32 v2, v2, s10, v184
	v_fma_f32 v3, v3, s10, v185
	v_fma_f32 v4, v4, s10, v186
	v_fma_f32 v5, v5, s10, v187
	v_cvt_pk_f16_f32 v2, v2, v3
	v_cvt_pk_f16_f32 v3, v4, v5
	v_bitop3_b32 v4, v95, v120, 12 bitop3:0x6c
	v_pk_fma_f32 v[18:19], v[18:19], s[10:11], v[184:185] op_sel_hi:[1,0,1]
	v_pk_fma_f32 v[20:21], v[20:21], s[10:11], v[186:187] op_sel_hi:[1,0,1]
	v_lshlrev_b32_e32 v4, 4, v4
	v_cvt_pk_f16_f32 v18, v18, v19
	v_cvt_pk_f16_f32 v19, v20, v21
	v_or_b32_e32 v5, v63, v4
	v_or_b32_e32 v4, v58, v4
	ds_write_b64 v5, v[18:19]
	ds_write_b64 v4, v[2:3]
	v_pk_fma_f32 v[2:3], v[22:23], s[10:11], v[188:189] op_sel_hi:[1,0,1]
	v_pk_fma_f32 v[4:5], v[6:7], s[10:11], v[188:189] op_sel_hi:[1,0,1]
	v_pk_fma_f32 v[6:7], v[24:25], s[10:11], v[190:191] op_sel_hi:[1,0,1]
	v_cvt_pk_f16_f32 v2, v2, v3
	v_cvt_pk_f16_f32 v3, v6, v7
	v_pk_fma_f32 v[6:7], v[8:9], s[10:11], v[190:191] op_sel_hi:[1,0,1]
	v_cvt_pk_f16_f32 v4, v4, v5
	v_cvt_pk_f16_f32 v5, v6, v7
	v_bitop3_b32 v6, v62, v120, 1 bitop3:0x36
	v_lshlrev_b32_e32 v6, 4, v6
	v_or_b32_e32 v7, v63, v6
	ds_write_b64 v7, v[2:3]
	v_or_b32_e32 v2, v58, v6
	ds_write_b64 v2, v[4:5]
	v_pk_fma_f32 v[2:3], v[26:27], s[10:11], v[192:193] op_sel_hi:[1,0,1]
	v_pk_fma_f32 v[6:7], v[28:29], s[10:11], v[194:195] op_sel_hi:[1,0,1]
	v_cvt_pk_f16_f32 v2, v2, v3
	v_pk_fma_f32 v[4:5], v[10:11], s[10:11], v[192:193] op_sel_hi:[1,0,1]
	v_cvt_pk_f16_f32 v3, v6, v7
	v_pk_fma_f32 v[6:7], v[12:13], s[10:11], v[194:195] op_sel_hi:[1,0,1]
	v_cvt_pk_f16_f32 v4, v4, v5
	v_cvt_pk_f16_f32 v5, v6, v7
	v_bitop3_b32 v6, v62, v120, 2 bitop3:0x36
	v_lshlrev_b32_e32 v6, 4, v6
	v_or_b32_e32 v7, v63, v6
	ds_write_b64 v7, v[2:3]
	v_or_b32_e32 v2, v58, v6
	ds_write_b64 v2, v[4:5]
	v_pk_fma_f32 v[2:3], v[30:31], s[10:11], v[196:197] op_sel_hi:[1,0,1]
	v_pk_fma_f32 v[6:7], v[32:33], s[10:11], v[198:199] op_sel_hi:[1,0,1]
	v_cvt_pk_f16_f32 v2, v2, v3
	v_pk_fma_f32 v[4:5], v[14:15], s[10:11], v[196:197] op_sel_hi:[1,0,1]
	v_cvt_pk_f16_f32 v3, v6, v7
	v_pk_fma_f32 v[6:7], v[16:17], s[10:11], v[198:199] op_sel_hi:[1,0,1]
	v_cvt_pk_f16_f32 v4, v4, v5
	v_cvt_pk_f16_f32 v5, v6, v7
	v_bitop3_b32 v6, v62, v120, 3 bitop3:0x36
	v_lshlrev_b32_e32 v6, 4, v6
	v_or_b32_e32 v7, v63, v6
	ds_write_b64 v7, v[2:3]
	v_or_b32_e32 v2, v58, v6
	ds_write_b64 v2, v[4:5]
	s_waitcnt vmcnt(0) lgkmcnt(0)
	s_barrier
	v_and_b32_e32 v236, 1, v101
	v_lshrrev_b32_e32 v237, 1, v101
	v_xor_b32_e32 v237, v237, v236
	v_lshl_or_b32 v236, v236, 1, v237
	v_lshrrev_b32_e32 v27, 8, v0
	v_lshrrev_b32_e32 v3, 3, v0
	v_and_b32_e32 v3, 16, v3
	v_mul_u32_u24_e32 v28, 0x60, v27
	v_lshlrev_b32_e32 v26, 5, v27
	v_or_b32_e32 v146, v3, v100
	v_or_b32_e32 v147, v28, v100
	v_or_b32_e32 v4, v146, v26
	v_lshlrev_b32_e32 v209, 2, v4
	v_add_u32_e32 v209, 0x27800, v209
	v_lshlrev_b32_e32 v4, 8, v4
	v_or_b32_e32 v5, 0x18000, v4
	v_bitop3_b32 v11, v236, v120, 12 bitop3:0x36
	v_or_b32_e32 v95, 0x1c000, v4
	v_lshlrev_b32_e32 v29, 3, v101
	v_bitop3_b32 v6, v236, v94, v61 bitop3:0x1e
	v_bitop3_b32 v8, v236, v120, 4 bitop3:0x36
	v_bitop3_b32 v10, v236, v120, 8 bitop3:0x36
	v_lshlrev_b32_e32 v94, 4, v11
	v_lshlrev_b32_e32 v6, 4, v6
	v_lshlrev_b32_e32 v8, 4, v8
	v_lshlrev_b32_e32 v58, 4, v10
	v_or_b32_e32 v7, v5, v6
	v_or_b32_e32 v9, v5, v8
	v_or_b32_e32 v10, v5, v58
	v_or_b32_e32 v5, v5, v94
	v_or_b32_e32 v6, v95, v6
	v_or_b32_e32 v60, v95, v8
	ds_read_b128 v[22:25], v7
	ds_read_b128 v[18:21], v9
	ds_read_b128 v[14:17], v10
	ds_read_b128 v[10:13], v5
	ds_read_b128 v[6:9], v6
	ds_read_b128 v[2:5], v60
	v_bfe_u32 v103, v0, 6, 1
	s_movk_i32 s5, 0x2000
	v_mad_u32_u24 v44, v103, 48, v147
	v_lshlrev_b32_e32 v60, 8, v44
	v_lshlrev_b32_e32 v44, 2, v44
	v_or_b32_e32 v35, v95, v58
	v_lshlrev_b32_e32 v58, 14, v99
	v_and_b32_e32 v44, 12, v44
	v_or_b32_e32 v56, v44, v61
	v_bitop3_b32 v44, v236, v44, v61 bitop3:0x1e
	v_lshl_add_u64 v[32:33], s[8:9], 0, v[58:59]
	v_lshlrev_b32_e32 v58, 4, v98
	v_or_b32_e32 v36, v95, v94
	v_lshl_add_u64 v[88:89], v[32:33], 0, v[58:59]
	v_lshl_or_b32 v57, v44, 4, v60
	ds_read_b128 v[40:43], v35
	ds_read_b128 v[106:109], v36
	s_load_dword s4, s[6:7], 0x0
	global_load_dwordx4 v[36:39], v[88:89], off
	global_load_dwordx4 v[32:35], v[88:89], off offset:1024
	ds_read_b128 v[44:47], v57
	v_bitop3_b32 v48, v236, v56, 4 bitop3:0x36
	v_lshl_or_b32 v62, v48, 4, v60
	ds_read_b128 v[48:51], v62
	v_bitop3_b32 v52, v236, v56, 8 bitop3:0x36
	v_lshl_or_b32 v63, v52, 4, v60
	ds_read_b128 v[52:55], v63
	s_waitcnt lgkmcnt(0)
	v_mfma_f32_16x16x32_f16 v[44:47], v[44:47], v[22:25], 0
	v_bitop3_b32 v64, v236, v56, 12 bitop3:0x36
	ds_read_b128 v[56:59], v57 offset:49152
	v_lshl_or_b32 v60, v64, 4, v60
	v_mfma_f32_16x16x32_f16 v[44:47], v[48:51], v[18:21], v[44:47]
	ds_read_b128 v[68:71], v60
	ds_read_b128 v[72:75], v62 offset:49152
	v_mad_u32_u24 v104, v103, 3, 1
	v_lshlrev_b32_e32 v132, 4, v104
	v_mfma_f32_16x16x32_f16 v[44:47], v[52:55], v[14:17], v[44:47]
	v_add_u32_e32 v52, v132, v147
	global_load_dwordx4 v[64:67], v[88:89], off offset:2048
	global_load_dwordx4 v[48:51], v[88:89], off offset:3072
	ds_read_b128 v[76:79], v63 offset:49152
	ds_read_b128 v[80:83], v60 offset:49152
	s_waitcnt lgkmcnt(3)
	v_mfma_f32_16x16x32_f16 v[44:47], v[68:71], v[10:13], v[44:47]
	v_lshlrev_b32_e32 v60, 8, v52
	v_lshlrev_b32_e32 v52, 2, v52
	v_and_b32_e32 v52, 12, v52
	v_mfma_f32_16x16x32_f16 v[44:47], v[56:59], v[6:9], v[44:47]
	v_or_b32_e32 v62, v52, v61
	v_bitop3_b32 v52, v236, v52, v61 bitop3:0x1e
	v_lshl_or_b32 v63, v52, 4, v60
	s_waitcnt lgkmcnt(2)
	v_mfma_f32_16x16x32_f16 v[44:47], v[72:75], v[2:5], v[44:47]
	ds_read_b128 v[52:55], v63
	v_bitop3_b32 v56, v236, v62, 4 bitop3:0x36
	v_lshl_or_b32 v84, v56, 4, v60
	s_waitcnt lgkmcnt(2)
	v_mfma_f32_16x16x32_f16 v[44:47], v[76:79], v[40:43], v[44:47]
	ds_read_b128 v[56:59], v84
	v_bitop3_b32 v68, v236, v62, 8 bitop3:0x36
	v_lshl_or_b32 v85, v68, 4, v60
	s_waitcnt lgkmcnt(2)
	v_mfma_f32_16x16x32_f16 v[110:113], v[80:83], v[106:109], v[44:47]
	ds_read_b128 v[68:71], v63 offset:49152
	v_bitop3_b32 v62, v236, v62, 12 bitop3:0x36
	v_lshl_or_b32 v60, v62, 4, v60
	ds_read_b128 v[44:47], v85
	s_waitcnt lgkmcnt(3)
	v_mfma_f32_16x16x32_f16 v[52:55], v[52:55], v[22:25], 0
	ds_read_b128 v[72:75], v60
	ds_read_b128 v[76:79], v84 offset:49152
	v_mad_u32_u24 v105, v103, 3, 2
	v_lshlrev_b32_e32 v133, 4, v105
	s_waitcnt lgkmcnt(4)
	v_mfma_f32_16x16x32_f16 v[52:55], v[56:59], v[18:21], v[52:55]
	ds_read_b128 v[56:59], v85 offset:49152
	v_add_co_u32_e32 v114, vcc, s15, v88
	s_waitcnt lgkmcnt(3)
	v_mfma_f32_16x16x32_f16 v[44:47], v[44:47], v[14:17], v[52:55]
	v_addc_co_u32_e32 v115, vcc, 0, v89, vcc
	s_waitcnt lgkmcnt(2)
	v_mfma_f32_16x16x32_f16 v[44:47], v[72:75], v[10:13], v[44:47]
	ds_read_b128 v[52:55], v60 offset:49152
	v_add_u32_e32 v60, v133, v147
	v_lshlrev_b32_e32 v72, 8, v60
	v_lshlrev_b32_e32 v60, 2, v60
	v_mfma_f32_16x16x32_f16 v[44:47], v[68:71], v[6:9], v[44:47]
	v_and_b32_e32 v60, 12, v60
	v_or_b32_e32 v68, v60, v61
	v_bitop3_b32 v60, v236, v60, v61 bitop3:0x1e
	v_lshl_or_b32 v69, v60, 4, v72
	s_waitcnt lgkmcnt(2)
	v_mfma_f32_16x16x32_f16 v[44:47], v[76:79], v[2:5], v[44:47]
	ds_read_b128 v[60:63], v69
	v_bitop3_b32 v70, v236, v68, 4 bitop3:0x36
	v_lshl_or_b32 v70, v70, 4, v72
	s_waitcnt lgkmcnt(2)
	v_mfma_f32_16x16x32_f16 v[44:47], v[56:59], v[40:43], v[44:47]
	ds_read_b128 v[56:59], v70
	v_bitop3_b32 v71, v236, v68, 8 bitop3:0x36
	v_lshl_or_b32 v71, v71, 4, v72
	s_waitcnt lgkmcnt(1)
	v_mfma_f32_16x16x32_f16 v[22:25], v[60:63], v[22:25], 0
	v_bitop3_b32 v60, v236, v68, 12 bitop3:0x36
	v_lshl_or_b32 v68, v60, 4, v72
	ds_read_b32 v210, v209
	v_mfma_f32_16x16x32_f16 v[126:129], v[52:55], v[106:109], v[44:47]
	s_nop 2
	ds_read_b128 v[44:47], v71
	ds_read_b128 v[52:55], v69 offset:49152
	ds_read_b128 v[60:63], v70 offset:49152
	s_waitcnt lgkmcnt(4)
	v_mfma_f32_16x16x32_f16 v[18:21], v[56:59], v[18:21], v[22:25]
	ds_read_b128 v[56:59], v71 offset:49152
	s_nop 1
	ds_read_b128 v[22:25], v68
	s_waitcnt lgkmcnt(4)
	v_mfma_f32_16x16x32_f16 v[14:17], v[44:47], v[14:17], v[18:21]
	v_add_co_u32_e32 v44, vcc, s5, v88
	s_movk_i32 s5, 0x3000
	s_nop 0
	ds_read_b128 v[18:21], v68 offset:49152
	s_waitcnt lgkmcnt(1)
	v_mfma_f32_16x16x32_f16 v[10:13], v[22:25], v[10:13], v[14:17]
	v_addc_co_u32_e32 v45, vcc, 0, v89, vcc
	global_load_dwordx4 v[84:87], v[114:115], off offset:1024
	global_load_dwordx4 v[80:83], v[114:115], off offset:2048
	global_load_dwordx4 v[92:95], v[44:45], off offset:-4096
	global_load_dwordx4 v[76:79], v[44:45], off
	v_mfma_f32_16x16x32_f16 v[6:9], v[52:55], v[6:9], v[10:13]
	global_load_dwordx4 v[72:75], v[44:45], off offset:1024
	global_load_dwordx4 v[68:71], v[44:45], off offset:2048
	global_load_dwordx4 v[52:55], v[44:45], off offset:3072
	v_mov_b32_e32 v13, 0xff61b1e6
	v_mfma_f32_16x16x32_f16 v[2:5], v[60:63], v[2:5], v[6:9]
	s_nop 2
	v_add_co_u32_e32 v6, vcc, s5, v88
	v_mfma_f32_16x16x32_f16 v[2:5], v[56:59], v[40:43], v[2:5]
	s_nop 0
	v_addc_co_u32_e32 v7, vcc, 0, v89, vcc
	global_load_dwordx4 v[88:91], v[114:115], off offset:3072
	global_load_dwordx4 v[60:63], v[6:7], off
	global_load_dwordx4 v[56:59], v[6:7], off offset:1024
	global_load_dwordx4 v[44:47], v[6:7], off offset:2048
	global_load_dwordx4 v[40:43], v[6:7], off offset:3072
	s_waitcnt lgkmcnt(0)
	v_mfma_f32_16x16x32_f16 v[16:19], v[18:21], v[106:109], v[2:5]
	s_mov_b32 s5, 0xff61b1e6
	s_nop 0
	v_or_b32_e32 v3, s14, v146
	v_mov_b32_e32 v4, 0x7df
	v_med3_u32 v3, v3, 32, v4
	v_or_b32_e32 v4, v97, v102
	v_sub_u32_e32 v3, v4, v3
	v_add_f32_e32 v2, s4, v210
	v_add_u32_e32 v3, 32, v3
	v_mad_u32_u24 v4, v103, 48, v3
	s_movk_i32 s4, 0x41
	v_add_f32_e32 v5, v2, v110
	v_mul_f32_e32 v5, 0x3db8aa3b, v5
	v_cmp_gt_u32_e32 vcc, s4, v4
	v_add_u32_e32 v6, 1, v4
	v_add_f32_e32 v7, v2, v111
	v_cndmask_b32_e32 v5, v13, v5, vcc
	v_mul_f32_e32 v7, 0x3db8aa3b, v7
	v_cmp_gt_u32_e32 vcc, s4, v6
	v_add_u32_e32 v8, 2, v4
	v_add_f32_e32 v9, v2, v112
	v_cndmask_b32_e32 v6, v13, v7, vcc
	v_mul_f32_e32 v9, 0x3db8aa3b, v9
	v_cmp_gt_u32_e32 vcc, s4, v8
	v_add_u32_e32 v4, 3, v4
	v_max3_f32 v7, v5, s5, v6
	v_cndmask_b32_e32 v8, v13, v9, vcc
	v_add_f32_e32 v9, v2, v113
	v_mul_f32_e32 v9, 0x3db8aa3b, v9
	v_cmp_gt_u32_e32 vcc, s4, v4
	v_add_u32_e32 v11, v3, v132
	v_add_f32_e32 v12, v2, v127
	v_cndmask_b32_e32 v10, v13, v9, vcc
	v_max3_f32 v4, v7, v8, v10
	v_add_f32_e32 v7, v2, v126
	v_mul_f32_e32 v7, 0x3db8aa3b, v7
	v_cmp_gt_u32_e32 vcc, s4, v11
	v_add_u32_e32 v9, 1, v11
	v_mul_f32_e32 v12, 0x3db8aa3b, v12
	v_cndmask_b32_e32 v7, v13, v7, vcc
	v_cmp_gt_u32_e32 vcc, s4, v9
	v_add_f32_e32 v14, v2, v128
	v_mul_f32_e32 v14, 0x3db8aa3b, v14
	v_cndmask_b32_e32 v9, v13, v12, vcc
	v_add_u32_e32 v12, 2, v11
	v_cmp_gt_u32_e32 vcc, s4, v12
	v_add_u32_e32 v11, 3, v11
	v_add_u32_e32 v3, v3, v133
	v_cndmask_b32_e32 v12, v13, v14, vcc
	v_add_f32_e32 v14, v2, v129
	v_mul_f32_e32 v14, 0x3db8aa3b, v14
	v_cmp_gt_u32_e32 vcc, s4, v11
	v_add_f32_e32 v11, v2, v16
	v_mul_f32_e32 v11, 0x3db8aa3b, v11
	v_cndmask_b32_e32 v15, v13, v14, vcc
	v_cmp_gt_u32_e32 vcc, s4, v3
	v_add_u32_e32 v14, 1, v3
	v_add_f32_e32 v16, v2, v17
	v_cndmask_b32_e32 v11, v13, v11, vcc
	v_mul_f32_e32 v16, 0x3db8aa3b, v16
	v_cmp_gt_u32_e32 vcc, s4, v14
	v_add_f32_e32 v17, v2, v18
	v_max3_f32 v4, v4, v7, v9
	v_cndmask_b32_e32 v14, v13, v16, vcc
	v_add_u32_e32 v16, 2, v3
	v_mul_f32_e32 v17, 0x3db8aa3b, v17
	v_cmp_gt_u32_e32 vcc, s4, v16
	v_add_u32_e32 v3, 3, v3
	v_add_f32_e32 v2, v2, v19
	v_max3_f32 v4, v4, v12, v15
	v_cndmask_b32_e32 v16, v13, v17, vcc
	v_mul_f32_e32 v2, 0x3db8aa3b, v2
	v_cmp_gt_u32_e32 vcc, s4, v3
	v_max3_f32 v4, v4, v11, v14
	v_lshlrev_b32_e32 v126, 5, v99
	v_cndmask_b32_e32 v17, v13, v2, vcc
	v_max3_f32 v2, v4, v16, v17
	v_mov_b32_e32 v3, v2
	v_lshlrev_b32_e32 v127, 2, v119
	v_lshrrev_b32_e32 v4, 7, v0
	v_cmp_gt_u32_e32 vcc, 16, v98
	v_permlane16_swap_b32_e32 v3, v2
	v_max_f32_e32 v2, v2, v3
	v_mov_b32_e32 v3, v2
	s_nop 1
	v_permlane32_swap_b32_e32 v3, v2
	v_max_f32_e32 v13, v2, v3
	v_and_b32_e32 v2, 0x180, v0
	v_or_b32_e32 v2, 0x23400, v2
	v_lshlrev_b32_e32 v3, 2, v100
	s_and_saveexec_b64 s[4:5], vcc
	v_lshlrev_b32_e32 v18, 6, v103
	v_add3_u32 v18, v2, v18, v3
	ds_write_b32 v18, v13
	s_or_b64 exec, exec, s[4:5]
	v_lshlrev_b32_e32 v18, 4, v103
	v_bitop3_b32 v19, v18, 16, v100 bitop3:0x36
	v_lshl_add_u32 v2, v19, 2, v2
	s_waitcnt lgkmcnt(0)
	s_barrier
	ds_read_b32 v19, v2
	v_max_f32_e32 v13, v13, v13
	v_mul_u32_u24_e32 v20, 0xd00, v4
	s_load_dwordx2 s[0:1], s[0:1], 0x30
	v_or_b32_e32 v2, 1, v124
	s_waitcnt lgkmcnt(0)
	v_max_f32_e32 v19, v19, v19
	v_max_f32_e32 v19, v13, v19
	v_sub_f32_e32 v5, v5, v19
	v_exp_f32_e32 v5, v5
	v_sub_f32_e32 v6, v6, v19
	v_exp_f32_e32 v6, v6
	v_sub_f32_e32 v8, v8, v19
	v_mul_u32_u24_e32 v13, 0xd0, v100
	v_exp_f32_e32 v8, v8
	v_sub_f32_e32 v10, v10, v19
	v_add3_u32 v20, v13, v20, v29
	v_exp_f32_e32 v10, v10
	v_or_b32_e32 v22, 0x20000, v20
	v_add_f32_e32 v20, 0, v5
	v_add_f32_e32 v20, v20, v6
	v_add_f32_e32 v20, v20, v8
	v_add_f32_e32 v23, v20, v10
	v_cvt_pk_f16_f32 v21, v8, v10
	v_cvt_pk_f16_f32 v20, v5, v6
	v_mad_u32_u24 v5, v103, s16, v22
	ds_write_b64 v5, v[20:21]
	v_sub_f32_e32 v5, v7, v19
	v_exp_f32_e32 v5, v5
	v_sub_f32_e32 v6, v9, v19
	v_exp_f32_e32 v6, v6
	v_sub_f32_e32 v7, v12, v19
	v_exp_f32_e32 v7, v7
	v_sub_f32_e32 v8, v15, v19
	v_exp_f32_e32 v8, v8
	v_sub_f32_e32 v10, v11, v19
	v_add_f32_e32 v9, v23, v5
	v_exp_f32_e32 v10, v10
	v_sub_f32_e32 v11, v14, v19
	v_add_f32_e32 v9, v9, v6
	v_exp_f32_e32 v11, v11
	v_sub_f32_e32 v12, v16, v19
	v_add_f32_e32 v9, v9, v7
	v_exp_f32_e32 v12, v12
	v_sub_f32_e32 v14, v17, v19
	v_add_f32_e32 v9, v9, v8
	v_exp_f32_e32 v14, v14
	v_add_f32_e32 v9, v9, v10
	v_add_f32_e32 v9, v9, v11
	v_add_f32_e32 v9, v9, v12
	v_add_f32_e32 v9, v9, v14
	v_mov_b32_e32 v15, v9
	v_cvt_pk_f16_f32 v7, v7, v8
	v_cvt_pk_f16_f32 v6, v5, v6
	v_lshl_add_u32 v5, v104, 5, v22
	ds_write_b64 v5, v[6:7]
	v_permlane16_swap_b32_e32 v15, v9
	v_add_f32_e32 v5, v9, v15
	v_mov_b32_e32 v6, v5
	s_movk_i32 s7, 0xd00
	s_mov_b32 s6, 0x20000
	v_cvt_pk_f16_f32 v9, v12, v14
	v_cvt_pk_f16_f32 v8, v10, v11
	v_lshl_add_u32 v7, v105, 5, v22
	ds_write_b64 v7, v[8:9]
	v_permlane32_swap_b32_e32 v6, v5
	s_and_saveexec_b64 s[4:5], vcc
	s_cbranch_execz .LBB1_4
	v_lshlrev_b32_e32 v4, 5, v4
	v_or_b32_e32 v7, v18, v100
	v_lshlrev_b32_e32 v4, 2, v4
	v_lshlrev_b32_e32 v7, 2, v7
	s_mov_b32 s8, 0x23600
	v_add3_u32 v4, v7, v4, s8
	v_add_f32_e32 v5, v5, v6
	ds_write_b32 v4, v5
